# NA units dealt by the XCD-consecutive virtual block index instead of blockIdx (adjacent row groups of one head share an XCD L2)
# speedup vs baseline: 1.0104x; 1.0104x over previous
; #define REP(x) for (int rep_ = 0; rep_ < ((DBL_PH) == (x) ? 2 : 1); ++rep_)
; __global__ void __launch_bounds__(NTHREADS, 2) fwd(const Params p) {
;     ...
;             { const int nun = 768 + (layer == 0 ? 12 : 0);
;               REP(32) for (int u = bid; u < nun; u += nb) { if (u < 768) { const int bh = u >> 6, rg = u & 63; na_unit(lp, layer, bh / 6, bh % 6, rg, false, lds); } else { const int bh = u - 768; na_unit(lp, layer, bh / 6, bh % 6, 0, true, lds); } } }
.LBB0_650:
	v_readlane_b32 s2, v254, 39
	v_mov_b32_e32 v219, 0xff61b1e6
	s_cmp_ge_i32 s2, s29
	s_cbranch_scc1 .LBB0_688
	v_readlane_b32 s2, v254, 63
	s_lshl_b32 s4, s2, 3
	s_mov_b32 s5, s31
	v_readlane_b32 s13, v254, 39
	s_nop 1
	s_lshl_b32 s12, s13, 2
	v_readlane_b32 s3, v255, 0
	s_branch .LBB0_654
